# diff attention row-sum on VALU instead of ones-MFMA; grid barrier between prologue P2 and layer-0 in-proj removed (no dependency)
# speedup vs baseline: 1.0204x; 1.0116x over previous
; #define PH_END   if (p + 1 < hi) xcd_barrier(bar, C.tid); else __syncthreads(); } ++p;
; __global__ void __launch_bounds__(NTHREADS, 2) mk_fwd(Args args) {
;     ...
;     PH_END
.LBB0_192:
	s_cmp_eq_u32 s93, s93
	s_mov_b64 s[4:5], -1
	s_cbranch_scc1 .LBB0_193
	s_getpc_b64 s[98:99]

; #define PH_END   if (p + 1 < hi) xcd_barrier(bar, C.tid); else __syncthreads(); } ++p;
; __global__ void __launch_bounds__(NTHREADS, 2) mk_fwd(Args args) {
;     ...
;     PH_END
.LBB0_1862:
	s_mov_b32 s82, s96
	s_barrier
	s_cmp_eq_u32 s93, s93
	s_mov_b64 s[4:5], -1
	s_cbranch_scc0 .LBB0_1863
	s_getpc_b64 s[98:99]
